# fp8 kernels: LDS-DMA completion waits moved to the phase before each first read (uniform counted vmcnt 8/10), five phases of latency cover instead of three
# speedup vs baseline: 1.0101x; 1.0056x over previous
.LBB3_3:
	s_waitcnt vmcnt(10)
	s_barrier
	s_setprio 1
	v_mfma_f32_16x16x128_f8f6f4 v[118:121], v[26:33], v[58:65], v[118:121]
	s_add_i32 s50, s50, 2
	s_add_u32 s10, s10, 0x100
	s_addc_u32 s11, s11, 0
	v_mfma_f32_16x16x128_f8f6f4 v[114:117], v[18:25], v[58:65], v[114:117]
	s_cmpk_eq_i32 s10, 0x700
	s_cselect_b64 s[18:19], -1, 0
	s_cmpk_lg_i32 s10, 0x700
	s_cselect_b64 s[26:27], -1, 0
	v_mfma_f32_16x16x128_f8f6f4 v[102:105], v[26:33], v[50:57], v[102:105]
	s_add_u32 s54, s48, s10
	s_addc_u32 s55, s49, s11
	s_add_u32 s51, s8, s10
	s_addc_u32 s52, s25, s11
	v_mfma_f32_16x16x128_f8f6f4 v[98:101], v[18:25], v[50:57], v[98:101]
	s_add_u32 s20, s51, 0x100
	s_addc_u32 s53, s52, 0
	s_add_u32 s12, s54, 0x100080
	s_addc_u32 s0, s55, 0
	v_mfma_f32_16x16x128_f8f6f4 v[86:89], v[26:33], v[42:49], v[86:89]
	s_and_b32 s13, s0, 0xffff
	s_cmp_gt_u32 s50, 13
	v_mfma_f32_16x16x128_f8f6f4 v[82:85], v[18:25], v[42:49], v[82:85]
	v_mfma_f32_16x16x128_f8f6f4 v[70:73], v[26:33], v[34:41], v[70:73]
	v_mfma_f32_16x16x128_f8f6f4 v[66:69], v[18:25], v[34:41], v[66:69]
	s_setprio 0
	s_barrier
	s_cbranch_scc1 .LBB3_20
.LBB3_4:
	ds_read_b128 v[2:5], v203
	ds_read_b128 v[10:13], v203 offset:2048
	ds_read_b128 v[6:9], v204
	ds_read_b128 v[14:17], v204 offset:2048
	s_mov_b32 m0, s46
	ds_read_b128 v[58:61], v200
	ds_read_b128 v[50:53], v200 offset:2048
	ds_read_b128 v[62:65], v201
	ds_read_b128 v[54:57], v201 offset:2048
	ds_read_b128 v[42:45], v200 offset:4096
	ds_read_b128 v[34:37], v200 offset:6144
	ds_read_b128 v[46:49], v201 offset:4096
	ds_read_b128 v[38:41], v201 offset:6144
	s_waitcnt vmcnt(8)
	buffer_load_dwordx4 v1, s[12:15], 0 offen lds
	s_mov_b32 m0, s47
	s_nop 0
	buffer_load_dwordx4 v195, s[12:15], 0 offen lds
	s_waitcnt lgkmcnt(8)
	s_barrier
	s_waitcnt lgkmcnt(0)
	s_setprio 1
	v_mfma_f32_16x16x128_f8f6f4 v[190:193], v[2:9], v[58:65], v[190:193]
	v_mfma_f32_16x16x128_f8f6f4 v[186:189], v[10:17], v[58:65], v[186:189]
	v_mfma_f32_16x16x128_f8f6f4 v[174:177], v[2:9], v[50:57], v[174:177]
	v_mfma_f32_16x16x128_f8f6f4 v[170:173], v[10:17], v[50:57], v[170:173]
	v_mfma_f32_16x16x128_f8f6f4 v[158:161], v[2:9], v[42:49], v[158:161]
	v_mfma_f32_16x16x128_f8f6f4 v[154:157], v[10:17], v[42:49], v[154:157]
	v_mfma_f32_16x16x128_f8f6f4 v[142:145], v[2:9], v[34:41], v[142:145]
	v_mfma_f32_16x16x128_f8f6f4 v[138:141], v[10:17], v[34:41], v[138:141]
	s_setprio 0
	s_barrier
	ds_read_b128 v[26:29], v205
	ds_read_b128 v[18:21], v205 offset:2048
	ds_read_b128 v[30:33], v206
	ds_read_b128 v[22:25], v206 offset:2048
	s_waitcnt vmcnt(8)
	s_and_b64 vcc, exec, s[18:19]
	s_cbranch_vccnz .LBB3_6
	s_and_b32 s21, s53, 0xffff
	s_mov_b32 s22, s14
	s_mov_b32 s23, s15
	s_mov_b32 m0, s33
	s_nop 0
	buffer_load_dwordx4 v194, s[20:23], 0 offen lds
	s_mov_b32 m0, s34
	s_nop 0
	buffer_load_dwordx4 v196, s[20:23], 0 offen lds

.LBB3_8:
	s_barrier
	s_waitcnt lgkmcnt(0)
	s_setprio 1
	v_mfma_f32_16x16x128_f8f6f4 v[126:129], v[2:9], v[58:65], v[126:129]
	v_mfma_f32_16x16x128_f8f6f4 v[122:125], v[10:17], v[58:65], v[122:125]
	v_mfma_f32_16x16x128_f8f6f4 v[110:113], v[2:9], v[50:57], v[110:113]
	v_mfma_f32_16x16x128_f8f6f4 v[106:109], v[10:17], v[50:57], v[106:109]
	v_mfma_f32_16x16x128_f8f6f4 v[94:97], v[2:9], v[42:49], v[94:97]
	v_mfma_f32_16x16x128_f8f6f4 v[90:93], v[10:17], v[42:49], v[90:93]
	v_mfma_f32_16x16x128_f8f6f4 v[78:81], v[2:9], v[34:41], v[78:81]
	v_mfma_f32_16x16x128_f8f6f4 v[74:77], v[10:17], v[34:41], v[74:77]
	s_setprio 0
	s_barrier
	s_and_b64 vcc, exec, s[0:1]
	s_mov_b64 s[22:23], -1
	s_cbranch_vccnz .LBB3_10
	s_add_u32 s56, s51, 0x10100
	s_addc_u32 s13, s52, 0
	s_mov_b32 m0, s17
	s_and_b32 s57, s13, 0xffff
	s_mov_b32 s58, s14
	s_mov_b32 s59, s15
	buffer_load_dwordx4 v194, s[56:59], 0 offen lds
	s_mov_b32 m0, s36
	s_mov_b64 s[22:23], 0
	buffer_load_dwordx4 v196, s[56:59], 0 offen lds
	s_waitcnt vmcnt(10)

.LBB3_12:
	s_barrier
	s_setprio 1
	v_mfma_f32_16x16x128_f8f6f4 v[118:121], v[26:33], v[58:65], v[118:121]
	s_add_i32 s13, 0, 0x18000
	v_add_u32_e32 v2, s13, v198
	v_add_u32_e32 v6, s13, v199
	v_mfma_f32_16x16x128_f8f6f4 v[114:117], v[18:25], v[58:65], v[114:117]
	v_mfma_f32_16x16x128_f8f6f4 v[102:105], v[26:33], v[50:57], v[102:105]
	v_mfma_f32_16x16x128_f8f6f4 v[98:101], v[18:25], v[50:57], v[98:101]
	v_mfma_f32_16x16x128_f8f6f4 v[86:89], v[26:33], v[42:49], v[86:89]
	v_mfma_f32_16x16x128_f8f6f4 v[82:85], v[18:25], v[42:49], v[82:85]
	v_mfma_f32_16x16x128_f8f6f4 v[70:73], v[26:33], v[34:41], v[70:73]
	v_mfma_f32_16x16x128_f8f6f4 v[66:69], v[18:25], v[34:41], v[66:69]
	s_setprio 0
	s_barrier
	ds_read_b128 v[10:13], v2
	ds_read_b128 v[2:5], v2 offset:2048
	ds_read_b128 v[14:17], v6
	ds_read_b128 v[6:9], v6 offset:2048
	ds_read_b128 v[58:61], v200 offset:32768
	ds_read_b128 v[50:53], v200 offset:34816
	ds_read_b128 v[62:65], v201 offset:32768
	ds_read_b128 v[54:57], v201 offset:34816
	ds_read_b128 v[42:45], v200 offset:36864
	ds_read_b128 v[34:37], v200 offset:38912
	ds_read_b128 v[46:49], v201 offset:36864
	ds_read_b128 v[38:41], v201 offset:38912
	s_waitcnt vmcnt(8)
	s_and_b64 vcc, exec, s[0:1]
	s_cbranch_vccnz .LBB3_14
	s_add_u32 s56, s54, 0x100100
	s_addc_u32 s13, s55, 0
	s_and_b32 s57, s13, 0xffff
	s_mov_b32 s58, s14
	s_mov_b32 s59, s15
	s_mov_b32 m0, s37
	s_nop 0
	buffer_load_dwordx4 v1, s[56:59], 0 offen lds
	s_mov_b32 m0, s38
	s_nop 0
	buffer_load_dwordx4 v195, s[56:59], 0 offen lds
.LBB3_14:
	s_waitcnt lgkmcnt(8)
	s_barrier
	s_waitcnt lgkmcnt(0)
	s_setprio 1
	v_mfma_f32_16x16x128_f8f6f4 v[190:193], v[10:17], v[58:65], v[190:193]
	v_mfma_f32_16x16x128_f8f6f4 v[186:189], v[2:9], v[58:65], v[186:189]
	v_mfma_f32_16x16x128_f8f6f4 v[174:177], v[10:17], v[50:57], v[174:177]
	v_mfma_f32_16x16x128_f8f6f4 v[170:173], v[2:9], v[50:57], v[170:173]
	v_mfma_f32_16x16x128_f8f6f4 v[158:161], v[10:17], v[42:49], v[158:161]
	v_mfma_f32_16x16x128_f8f6f4 v[154:157], v[2:9], v[42:49], v[154:157]
	v_mfma_f32_16x16x128_f8f6f4 v[142:145], v[10:17], v[34:41], v[142:145]
	v_mfma_f32_16x16x128_f8f6f4 v[138:141], v[2:9], v[34:41], v[138:141]
	s_setprio 0
	s_barrier
	s_add_i32 s13, 0, 0x1c000
	v_add_u32_e32 v18, s13, v198
	v_add_u32_e32 v22, s13, v199
	ds_read_b128 v[26:29], v18
	ds_read_b128 v[18:21], v18 offset:2048
	ds_read_b128 v[30:33], v22
	ds_read_b128 v[22:25], v22 offset:2048
	s_waitcnt vmcnt(8)
	s_and_b64 vcc, exec, s[0:1]
	s_cbranch_vccnz .LBB3_16
	s_and_b64 s[22:23], exec, s[18:19]
	s_cselect_b32 s20, s8, s20
	s_cselect_b32 s13, s25, s53
	s_add_u32 s56, s20, 0x80
	s_addc_u32 s13, s13, 0
	s_and_b32 s57, s13, 0xffff
	s_mov_b32 s58, s14
	s_mov_b32 s59, s15
	s_mov_b32 m0, s40
	s_nop 0
	buffer_load_dwordx4 v194, s[56:59], 0 offen lds
	s_mov_b32 m0, s41
	s_nop 0
	buffer_load_dwordx4 v196, s[56:59], 0 offen lds

.LBB4_13:
	s_waitcnt vmcnt(10)
	s_barrier
	s_setprio 1
	v_mfma_f32_16x16x128_f8f6f4 v[116:119], v[24:31], v[56:63], v[116:119]
	s_add_i32 s44, s44, 2
	s_add_u32 s10, s10, 0x100
	s_addc_u32 s11, s11, 0
	v_mfma_f32_16x16x128_f8f6f4 v[112:115], v[16:23], v[56:63], v[112:115]
	s_cmpk_eq_i32 s10, 0x700
	s_cselect_b64 s[18:19], -1, 0
	s_cmpk_lg_i32 s10, 0x700
	s_cselect_b64 s[24:25], -1, 0
	v_mfma_f32_16x16x128_f8f6f4 v[100:103], v[24:31], v[48:55], v[100:103]
	s_add_u32 s49, s16, s10
	s_addc_u32 s50, s9, s11
	s_add_u32 s46, s8, s10
	s_addc_u32 s47, s3, s11
	v_mfma_f32_16x16x128_f8f6f4 v[96:99], v[16:23], v[48:55], v[96:99]
	s_add_u32 s20, s46, 0x100
	s_addc_u32 s48, s47, 0
	s_add_u32 s12, s49, 0x40080
	s_addc_u32 s0, s50, 0
	v_mfma_f32_16x16x128_f8f6f4 v[84:87], v[24:31], v[40:47], v[84:87]
	s_and_b32 s13, s0, 0xffff
	s_cmp_gt_u32 s44, 13
	v_mfma_f32_16x16x128_f8f6f4 v[80:83], v[16:23], v[40:47], v[80:83]
	v_mfma_f32_16x16x128_f8f6f4 v[68:71], v[24:31], v[32:39], v[68:71]
	v_mfma_f32_16x16x128_f8f6f4 v[64:67], v[16:23], v[32:39], v[64:67]
	s_setprio 0
	s_barrier
	s_cbranch_scc1 .LBB4_30
.LBB4_14:
	ds_read_b128 v[0:3], v202
	ds_read_b128 v[8:11], v202 offset:2048
	ds_read_b128 v[4:7], v203
	ds_read_b128 v[12:15], v203 offset:2048
	s_mov_b32 m0, s42
	ds_read_b128 v[56:59], v200
	ds_read_b128 v[48:51], v200 offset:2048
	ds_read_b128 v[60:63], v201
	ds_read_b128 v[52:55], v201 offset:2048
	ds_read_b128 v[40:43], v200 offset:4096
	ds_read_b128 v[32:35], v200 offset:6144
	ds_read_b128 v[44:47], v201 offset:4096
	ds_read_b128 v[36:39], v201 offset:6144
	s_waitcnt vmcnt(8)
	buffer_load_dwordx4 v192, s[12:15], 0 offen lds
	s_mov_b32 m0, s43
	s_nop 0
	buffer_load_dwordx4 v194, s[12:15], 0 offen lds
	s_waitcnt lgkmcnt(8)
	s_barrier
	s_waitcnt lgkmcnt(0)
	s_setprio 1
	v_mfma_f32_16x16x128_f8f6f4 v[188:191], v[0:7], v[56:63], v[188:191]
	v_mfma_f32_16x16x128_f8f6f4 v[184:187], v[8:15], v[56:63], v[184:187]
	v_mfma_f32_16x16x128_f8f6f4 v[172:175], v[0:7], v[48:55], v[172:175]
	v_mfma_f32_16x16x128_f8f6f4 v[168:171], v[8:15], v[48:55], v[168:171]
	v_mfma_f32_16x16x128_f8f6f4 v[156:159], v[0:7], v[40:47], v[156:159]
	v_mfma_f32_16x16x128_f8f6f4 v[152:155], v[8:15], v[40:47], v[152:155]
	v_mfma_f32_16x16x128_f8f6f4 v[140:143], v[0:7], v[32:39], v[140:143]
	v_mfma_f32_16x16x128_f8f6f4 v[136:139], v[8:15], v[32:39], v[136:139]
	s_setprio 0
	s_barrier
	ds_read_b128 v[24:27], v204
	ds_read_b128 v[16:19], v204 offset:2048
	ds_read_b128 v[28:31], v205
	ds_read_b128 v[20:23], v205 offset:2048
	s_waitcnt vmcnt(8)
	s_and_b64 vcc, exec, s[18:19]
	s_cbranch_vccnz .LBB4_16
	s_and_b32 s21, s48, 0xffff
	s_mov_b32 s22, s14
	s_mov_b32 s23, s15
	s_mov_b32 m0, s28
	s_nop 0
	buffer_load_dwordx4 v193, s[20:23], 0 offen lds
	s_mov_b32 m0, s29
	s_nop 0
	buffer_load_dwordx4 v195, s[20:23], 0 offen lds

.LBB4_18:
	s_barrier
	s_waitcnt lgkmcnt(0)
	s_setprio 1
	v_mfma_f32_16x16x128_f8f6f4 v[124:127], v[0:7], v[56:63], v[124:127]
	v_mfma_f32_16x16x128_f8f6f4 v[120:123], v[8:15], v[56:63], v[120:123]
	v_mfma_f32_16x16x128_f8f6f4 v[108:111], v[0:7], v[48:55], v[108:111]
	v_mfma_f32_16x16x128_f8f6f4 v[104:107], v[8:15], v[48:55], v[104:107]
	v_mfma_f32_16x16x128_f8f6f4 v[92:95], v[0:7], v[40:47], v[92:95]
	v_mfma_f32_16x16x128_f8f6f4 v[88:91], v[8:15], v[40:47], v[88:91]
	v_mfma_f32_16x16x128_f8f6f4 v[76:79], v[0:7], v[32:39], v[76:79]
	v_mfma_f32_16x16x128_f8f6f4 v[72:75], v[8:15], v[32:39], v[72:75]
	s_setprio 0
	s_barrier
	s_and_b64 vcc, exec, s[0:1]
	s_mov_b64 s[22:23], -1
	s_cbranch_vccnz .LBB4_20
	s_add_u32 s52, s46, 0x4100
	s_addc_u32 s13, s47, 0
	s_mov_b32 m0, s17
	s_and_b32 s53, s13, 0xffff
	s_mov_b32 s54, s14
	s_mov_b32 s55, s15
	buffer_load_dwordx4 v193, s[52:55], 0 offen lds
	s_mov_b32 m0, s31
	s_mov_b64 s[22:23], 0
	buffer_load_dwordx4 v195, s[52:55], 0 offen lds
	s_waitcnt vmcnt(10)

.LBB4_22:
	s_barrier
	s_setprio 1
	v_mfma_f32_16x16x128_f8f6f4 v[116:119], v[24:31], v[56:63], v[116:119]
	v_add_u32_e32 v0, s45, v198
	v_add_u32_e32 v4, s45, v199
	v_mfma_f32_16x16x128_f8f6f4 v[112:115], v[16:23], v[56:63], v[112:115]
	v_mfma_f32_16x16x128_f8f6f4 v[100:103], v[24:31], v[48:55], v[100:103]
	v_mfma_f32_16x16x128_f8f6f4 v[96:99], v[16:23], v[48:55], v[96:99]
	v_mfma_f32_16x16x128_f8f6f4 v[84:87], v[24:31], v[40:47], v[84:87]
	v_mfma_f32_16x16x128_f8f6f4 v[80:83], v[16:23], v[40:47], v[80:83]
	v_mfma_f32_16x16x128_f8f6f4 v[68:71], v[24:31], v[32:39], v[68:71]
	v_mfma_f32_16x16x128_f8f6f4 v[64:67], v[16:23], v[32:39], v[64:67]
	s_setprio 0
	s_barrier
	ds_read_b128 v[8:11], v0
	ds_read_b128 v[0:3], v0 offset:2048
	ds_read_b128 v[12:15], v4
	ds_read_b128 v[4:7], v4 offset:2048
	ds_read_b128 v[56:59], v200 offset:32768
	ds_read_b128 v[48:51], v200 offset:34816
	ds_read_b128 v[60:63], v201 offset:32768
	ds_read_b128 v[52:55], v201 offset:34816
	ds_read_b128 v[40:43], v200 offset:36864
	ds_read_b128 v[32:35], v200 offset:38912
	ds_read_b128 v[44:47], v201 offset:36864
	ds_read_b128 v[36:39], v201 offset:38912
	s_waitcnt vmcnt(8)
	s_and_b64 vcc, exec, s[0:1]
	s_cbranch_vccnz .LBB4_24
	s_add_u32 s52, s49, 0x40100
	s_addc_u32 s13, s50, 0
	s_and_b32 s53, s13, 0xffff
	s_mov_b32 s54, s14
	s_mov_b32 s55, s15
	s_mov_b32 m0, s34
	s_nop 0
	buffer_load_dwordx4 v192, s[52:55], 0 offen lds
	s_mov_b32 m0, s35
	s_nop 0
	buffer_load_dwordx4 v194, s[52:55], 0 offen lds
.LBB4_24:
	s_waitcnt lgkmcnt(8)
	s_barrier
	s_waitcnt lgkmcnt(0)
	s_setprio 1
	v_mfma_f32_16x16x128_f8f6f4 v[188:191], v[8:15], v[56:63], v[188:191]
	v_mfma_f32_16x16x128_f8f6f4 v[184:187], v[0:7], v[56:63], v[184:187]
	v_mfma_f32_16x16x128_f8f6f4 v[172:175], v[8:15], v[48:55], v[172:175]
	v_mfma_f32_16x16x128_f8f6f4 v[168:171], v[0:7], v[48:55], v[168:171]
	v_mfma_f32_16x16x128_f8f6f4 v[156:159], v[8:15], v[40:47], v[156:159]
	v_mfma_f32_16x16x128_f8f6f4 v[152:155], v[0:7], v[40:47], v[152:155]
	v_mfma_f32_16x16x128_f8f6f4 v[140:143], v[8:15], v[32:39], v[140:143]
	v_mfma_f32_16x16x128_f8f6f4 v[136:139], v[0:7], v[32:39], v[136:139]
	s_setprio 0
	s_barrier
	s_add_i32 s13, 0, 0x1c000
	v_add_u32_e32 v16, s13, v198
	v_add_u32_e32 v20, s13, v199
	ds_read_b128 v[24:27], v16
	ds_read_b128 v[16:19], v16 offset:2048
	ds_read_b128 v[28:31], v20
	ds_read_b128 v[20:23], v20 offset:2048
	s_waitcnt vmcnt(8)
	s_and_b64 vcc, exec, s[0:1]
	s_cbranch_vccnz .LBB4_26
	s_and_b64 s[22:23], exec, s[18:19]
	s_cselect_b32 s20, s8, s20
	s_cselect_b32 s13, s3, s48
	s_add_u32 s48, s20, 0x80
	s_addc_u32 s13, s13, 0
	s_and_b32 s49, s13, 0xffff
	s_mov_b32 s50, s14
	s_mov_b32 s51, s15
	s_mov_b32 m0, s36
	s_nop 0
	buffer_load_dwordx4 v193, s[48:51], 0 offen lds
	s_mov_b32 m0, s37
	s_nop 0
	buffer_load_dwordx4 v195, s[48:51], 0 offen lds

.LBB5_17:
	s_waitcnt vmcnt(10)
	s_barrier
	s_setprio 1
	v_mfma_f32_16x16x128_f8f6f4 v[108:111], v[24:31], v[56:63], v[108:111]
	s_add_i32 s45, s45, 2
	s_add_u32 s14, s14, 0x100
	s_addc_u32 s15, s15, 0
	v_mfma_f32_16x16x128_f8f6f4 v[104:107], v[16:23], v[56:63], v[104:107]
	s_cmpk_eq_i32 s14, 0x700
	s_cselect_b64 s[18:19], -1, 0
	s_cmpk_lg_i32 s14, 0x700
	s_cselect_b64 s[26:27], -1, 0
	v_mfma_f32_16x16x128_f8f6f4 v[92:95], v[24:31], v[48:55], v[92:95]
	s_add_u32 s50, s16, s14
	s_addc_u32 s51, s13, s15
	s_add_u32 s47, s12, s14
	s_addc_u32 s48, s7, s15
	v_mfma_f32_16x16x128_f8f6f4 v[88:91], v[16:23], v[48:55], v[88:91]
	s_add_u32 s20, s47, 0x100
	s_addc_u32 s49, s48, 0
	s_add_u32 s8, s50, 0x40080
	s_addc_u32 s0, s51, 0
	v_mfma_f32_16x16x128_f8f6f4 v[80:83], v[24:31], v[40:47], v[80:83]
	s_and_b32 s9, s0, 0xffff
	s_cmp_gt_u32 s45, 13
	v_mfma_f32_16x16x128_f8f6f4 v[76:79], v[16:23], v[40:47], v[76:79]
	v_mfma_f32_16x16x128_f8f6f4 v[68:71], v[24:31], v[32:39], v[68:71]
	v_mfma_f32_16x16x128_f8f6f4 v[64:67], v[16:23], v[32:39], v[64:67]
	s_setprio 0
	s_barrier
	s_cbranch_scc1 .LBB5_34
.LBB5_18:
	ds_read_b128 v[0:3], v200
	ds_read_b128 v[8:11], v200 offset:2048
	ds_read_b128 v[4:7], v201
	ds_read_b128 v[12:15], v201 offset:2048
	s_mov_b32 m0, s43
	ds_read_b128 v[56:59], v198
	ds_read_b128 v[48:51], v198 offset:2048
	ds_read_b128 v[60:63], v199
	ds_read_b128 v[52:55], v199 offset:2048
	ds_read_b128 v[40:43], v198 offset:4096
	ds_read_b128 v[32:35], v198 offset:6144
	ds_read_b128 v[44:47], v199 offset:4096
	ds_read_b128 v[36:39], v199 offset:6144
	s_waitcnt vmcnt(8)
	buffer_load_dwordx4 v192, s[8:11], 0 offen lds
	s_mov_b32 m0, s44
	s_nop 0
	buffer_load_dwordx4 v193, s[8:11], 0 offen lds
	s_waitcnt lgkmcnt(8)
	s_barrier
	s_waitcnt lgkmcnt(0)
	s_setprio 1
	v_mfma_f32_16x16x128_f8f6f4 v[188:191], v[0:7], v[56:63], v[188:191]
	v_mfma_f32_16x16x128_f8f6f4 v[184:187], v[8:15], v[56:63], v[184:187]
	v_mfma_f32_16x16x128_f8f6f4 v[176:179], v[0:7], v[48:55], v[176:179]
	v_mfma_f32_16x16x128_f8f6f4 v[168:171], v[8:15], v[48:55], v[168:171]
	v_mfma_f32_16x16x128_f8f6f4 v[160:163], v[0:7], v[40:47], v[160:163]
	v_mfma_f32_16x16x128_f8f6f4 v[152:155], v[8:15], v[40:47], v[152:155]
	v_mfma_f32_16x16x128_f8f6f4 v[144:147], v[0:7], v[32:39], v[144:147]
	v_mfma_f32_16x16x128_f8f6f4 v[136:139], v[8:15], v[32:39], v[136:139]
	s_setprio 0
	s_barrier
	ds_read_b128 v[24:27], v202
	ds_read_b128 v[16:19], v202 offset:2048
	ds_read_b128 v[28:31], v203
	ds_read_b128 v[20:23], v203 offset:2048
	s_waitcnt vmcnt(8)
	s_and_b64 vcc, exec, s[18:19]
	s_cbranch_vccnz .LBB5_20
	s_and_b32 s21, s49, 0xffff
	s_mov_b32 s22, s10
	s_mov_b32 s23, s11
	s_mov_b32 m0, s29
	s_nop 0
	buffer_load_dwordx4 v192, s[20:23], 0 offen lds
	s_mov_b32 m0, s30
	s_nop 0
	buffer_load_dwordx4 v193, s[20:23], 0 offen lds

.LBB5_22:
	s_barrier
	s_waitcnt lgkmcnt(0)
	s_setprio 1
	v_mfma_f32_16x16x128_f8f6f4 v[124:127], v[0:7], v[56:63], v[124:127]
	v_mfma_f32_16x16x128_f8f6f4 v[120:123], v[8:15], v[56:63], v[120:123]
	v_mfma_f32_16x16x128_f8f6f4 v[116:119], v[0:7], v[48:55], v[116:119]
	v_mfma_f32_16x16x128_f8f6f4 v[112:115], v[8:15], v[48:55], v[112:115]
	v_mfma_f32_16x16x128_f8f6f4 v[100:103], v[0:7], v[40:47], v[100:103]
	v_mfma_f32_16x16x128_f8f6f4 v[96:99], v[8:15], v[40:47], v[96:99]
	v_mfma_f32_16x16x128_f8f6f4 v[84:87], v[0:7], v[32:39], v[84:87]
	v_mfma_f32_16x16x128_f8f6f4 v[72:75], v[8:15], v[32:39], v[72:75]
	s_setprio 0
	s_barrier
	s_and_b64 vcc, exec, s[0:1]
	s_mov_b64 s[22:23], -1
	s_cbranch_vccnz .LBB5_24
	s_add_u32 s52, s47, 0x40100
	s_addc_u32 s9, s48, 0
	s_mov_b32 m0, s17
	s_and_b32 s53, s9, 0xffff
	s_mov_b32 s54, s10
	s_mov_b32 s55, s11
	buffer_load_dwordx4 v192, s[52:55], 0 offen lds
	s_mov_b32 m0, s33
	s_mov_b64 s[22:23], 0
	buffer_load_dwordx4 v193, s[52:55], 0 offen lds
	s_waitcnt vmcnt(10)

.LBB5_26:
	s_barrier
	s_setprio 1
	v_mfma_f32_16x16x128_f8f6f4 v[108:111], v[24:31], v[56:63], v[108:111]
	v_add_u32_e32 v0, s46, v196
	v_add_u32_e32 v4, s46, v197
	v_mfma_f32_16x16x128_f8f6f4 v[104:107], v[16:23], v[56:63], v[104:107]
	v_mfma_f32_16x16x128_f8f6f4 v[92:95], v[24:31], v[48:55], v[92:95]
	v_mfma_f32_16x16x128_f8f6f4 v[88:91], v[16:23], v[48:55], v[88:91]
	v_mfma_f32_16x16x128_f8f6f4 v[80:83], v[24:31], v[40:47], v[80:83]
	v_mfma_f32_16x16x128_f8f6f4 v[76:79], v[16:23], v[40:47], v[76:79]
	v_mfma_f32_16x16x128_f8f6f4 v[68:71], v[24:31], v[32:39], v[68:71]
	v_mfma_f32_16x16x128_f8f6f4 v[64:67], v[16:23], v[32:39], v[64:67]
	s_setprio 0
	s_barrier
	ds_read_b128 v[8:11], v0
	ds_read_b128 v[0:3], v0 offset:2048
	ds_read_b128 v[12:15], v4
	ds_read_b128 v[4:7], v4 offset:2048
	ds_read_b128 v[56:59], v198 offset:32768
	ds_read_b128 v[48:51], v198 offset:34816
	ds_read_b128 v[60:63], v199 offset:32768
	ds_read_b128 v[52:55], v199 offset:34816
	ds_read_b128 v[40:43], v198 offset:36864
	ds_read_b128 v[32:35], v198 offset:38912
	ds_read_b128 v[44:47], v199 offset:36864
	ds_read_b128 v[36:39], v199 offset:38912
	s_waitcnt vmcnt(8)
	s_and_b64 vcc, exec, s[0:1]
	s_cbranch_vccnz .LBB5_28
	s_add_u32 s52, s50, 0x40100
	s_addc_u32 s9, s51, 0
	s_and_b32 s53, s9, 0xffff
	s_mov_b32 s54, s10
	s_mov_b32 s55, s11
	s_mov_b32 m0, s34
	s_nop 0
	buffer_load_dwordx4 v192, s[52:55], 0 offen lds
	s_mov_b32 m0, s36
	s_nop 0
	buffer_load_dwordx4 v193, s[52:55], 0 offen lds
.LBB5_28:
	s_waitcnt lgkmcnt(8)
	s_barrier
	s_waitcnt lgkmcnt(0)
	s_setprio 1
	v_mfma_f32_16x16x128_f8f6f4 v[188:191], v[8:15], v[56:63], v[188:191]
	v_mfma_f32_16x16x128_f8f6f4 v[184:187], v[0:7], v[56:63], v[184:187]
	v_mfma_f32_16x16x128_f8f6f4 v[176:179], v[8:15], v[48:55], v[176:179]
	v_mfma_f32_16x16x128_f8f6f4 v[168:171], v[0:7], v[48:55], v[168:171]
	v_mfma_f32_16x16x128_f8f6f4 v[160:163], v[8:15], v[40:47], v[160:163]
	v_mfma_f32_16x16x128_f8f6f4 v[152:155], v[0:7], v[40:47], v[152:155]
	v_mfma_f32_16x16x128_f8f6f4 v[144:147], v[8:15], v[32:39], v[144:147]
	v_mfma_f32_16x16x128_f8f6f4 v[136:139], v[0:7], v[32:39], v[136:139]
	s_setprio 0
	s_barrier
	s_add_i32 s9, 0, 0x1c000
	v_add_u32_e32 v16, s9, v196
	v_add_u32_e32 v20, s9, v197
	ds_read_b128 v[24:27], v16
	ds_read_b128 v[16:19], v16 offset:2048
	ds_read_b128 v[28:31], v20
	ds_read_b128 v[20:23], v20 offset:2048
	s_waitcnt vmcnt(8)
	s_and_b64 vcc, exec, s[0:1]
	s_cbranch_vccnz .LBB5_30
	s_and_b64 s[22:23], exec, s[18:19]
	s_cselect_b32 s20, s12, s20
	s_cselect_b32 s9, s7, s49
	s_add_u32 s52, s20, 0x80
	s_addc_u32 s9, s9, 0
	s_and_b32 s53, s9, 0xffff
	s_mov_b32 s54, s10
	s_mov_b32 s55, s11
	s_mov_b32 m0, s37
	s_nop 0
	buffer_load_dwordx4 v192, s[52:55], 0 offen lds
	s_mov_b32 m0, s38
	s_nop 0
	buffer_load_dwordx4 v193, s[52:55], 0 offen lds
